# speedup vs baseline: 1.0149x; 1.0149x over previous
.LBB1_8:
	s_or_b64 exec, exec, s[4:5]
	v_add_u32_e32 v10, v172, v2
	s_waitcnt vmcnt(1) lgkmcnt(0)
	s_barrier
	ds_read_b128 v[18:21], v10 offset:256
	ds_read_b128 v[22:25], v10 offset:288
	ds_read_b128 v[82:85], v10 offset:320
	ds_read_b128 v[86:89], v10 offset:352
	ds_read_b128 v[74:77], v10 offset:384
	ds_read_b128 v[78:81], v10 offset:416
	ds_read_b128 v[2:5], v213 offset:32768
	ds_read_b128 v[6:9], v213 offset:0
	ds_read_b128 v[66:69], v10 offset:448
	ds_read_b128 v[70:73], v10 offset:480
	ds_read_b128 v[10:13], v213 offset:1024
	s_waitcnt lgkmcnt(3)
	v_pk_mul_f32 v[26:27], v[8:9], v[20:21]
	v_pk_mul_f32 v[28:29], v[6:7], v[18:19]
	ds_read_b128 v[14:17], v213 offset:8192
	s_waitcnt lgkmcnt(1)
	v_pk_mul_f32 v[12:13], v[12:13], v[24:25]
	v_pk_mul_f32 v[10:11], v[10:11], v[22:23]
	v_pk_fma_f32 v[30:31], v[8:9], v[20:21], v[12:13]
	v_pk_fma_f32 v[32:33], v[6:7], v[18:19], v[10:11]
	v_cvt_pk_bf16_f32 v9, v12, v13
	v_cvt_pk_bf16_f32 v7, v26, v27
	v_cvt_pk_bf16_f32 v8, v10, v11
	v_cvt_pk_bf16_f32 v6, v28, v29
	ds_read_b128 v[10:13], v213 offset:33792
	s_nop 0
	v_mfma_f32_32x32x16_bf16 v[34:49], v[2:5], v[6:9], 0
	ds_read_b128 v[6:9], v213 offset:9216
	s_waitcnt lgkmcnt(2)
	v_mul_f32_e32 v26, v16, v20
	v_mul_f32_e32 v27, v17, v21
	v_pk_mul_f32 v[50:51], v[14:15], v[18:19]
	s_mov_b32 s4, 0x3727c5ac
	s_waitcnt lgkmcnt(0)
	v_pk_mul_f32 v[8:9], v[8:9], v[24:25]
	v_pk_mul_f32 v[28:29], v[6:7], v[22:23]
	v_pk_fma_f32 v[90:91], v[16:17], v[20:21], v[8:9]
	v_pk_fma_f32 v[92:93], v[14:15], v[18:19], v[28:29]
	ds_read_b128 v[14:17], v213 offset:2048
	v_cvt_pk_bf16_f32 v9, v8, v9
	v_cvt_pk_bf16_f32 v7, v26, v27
	v_cvt_pk_bf16_f32 v8, v28, v29
	ds_read_b128 v[26:29], v213 offset:3072
	v_cvt_pk_bf16_f32 v6, v50, v51
	s_waitcnt lgkmcnt(1)
	v_pk_mul_f32 v[94:95], v[14:15], v[82:83]
	s_mov_b32 s0, 0x3c800000
	v_mfma_f32_32x32x16_bf16 v[50:65], v[2:5], v[6:9], 0
	v_mul_f32_e32 v2, v16, v84
	v_mul_f32_e32 v3, v17, v85
	s_waitcnt lgkmcnt(0)
	v_mul_f32_e32 v4, v28, v88
	v_mul_f32_e32 v5, v29, v89
	v_pk_mul_f32 v[6:7], v[26:27], v[86:87]
	v_pk_fma_f32 v[8:9], v[16:17], v[84:85], v[4:5]
	v_cvt_pk_bf16_f32 v3, v2, v3
	v_pk_fma_f32 v[14:15], v[14:15], v[82:83], v[6:7]
	v_pk_add_f32 v[26:27], v[8:9], v[30:31]
	v_cvt_pk_bf16_f32 v5, v4, v5
	v_cvt_pk_bf16_f32 v4, v6, v7
	ds_read_b128 v[6:9], v213 offset:10240
	v_pk_add_f32 v[28:29], v[14:15], v[32:33]
	ds_read_b128 v[14:17], v213 offset:11264
	v_cvt_pk_bf16_f32 v2, v94, v95
	s_waitcnt lgkmcnt(1)
	v_pk_mul_f32 v[30:31], v[6:7], v[82:83]
	v_mov_b64_e32 v[152:153], s[4:5]
	v_mfma_f32_32x32x16_bf16 v[34:49], v[10:13], v[2:5], v[34:49]
	v_mul_f32_e32 v2, v8, v84
	v_mul_f32_e32 v3, v9, v85
	s_waitcnt lgkmcnt(0)
	v_mul_f32_e32 v4, v16, v88
	v_mul_f32_e32 v5, v17, v89
	v_pk_mul_f32 v[14:15], v[14:15], v[86:87]
	v_pk_fma_f32 v[8:9], v[8:9], v[84:85], v[4:5]
	v_pk_fma_f32 v[6:7], v[6:7], v[82:83], v[14:15]
	v_cvt_pk_bf16_f32 v5, v4, v5
	v_cvt_pk_bf16_f32 v3, v2, v3
	v_cvt_pk_bf16_f32 v4, v14, v15
	v_pk_add_f32 v[32:33], v[8:9], v[90:91]
	v_pk_add_f32 v[90:91], v[6:7], v[92:93]
	ds_read_b128 v[6:9], v213 offset:34816
	ds_read_b128 v[14:17], v213 offset:4096
	v_cvt_pk_bf16_f32 v2, v30, v31
	s_mov_b32 s13, 0
	s_mov_b64 s[6:7], 0
	v_mfma_f32_32x32x16_bf16 v[50:65], v[10:13], v[2:5], v[50:65]
	ds_read_b128 v[2:5], v213 offset:5120
	ds_read_b128 v[10:13], v213 offset:12288
	s_waitcnt lgkmcnt(2)
	v_pk_mul_f32 v[30:31], v[16:17], v[76:77]
	v_pk_mul_f32 v[92:93], v[14:15], v[74:75]
	s_waitcnt lgkmcnt(1)
	v_pk_mul_f32 v[4:5], v[4:5], v[80:81]
	v_pk_mul_f32 v[94:95], v[2:3], v[78:79]
	v_pk_fma_f32 v[2:3], v[16:17], v[76:77], v[4:5]
	v_cvt_pk_bf16_f32 v5, v4, v5
	v_pk_add_f32 v[96:97], v[2:3], v[26:27]
	v_cvt_pk_bf16_f32 v3, v30, v31
	v_cvt_pk_bf16_f32 v4, v94, v95
	v_cvt_pk_bf16_f32 v2, v92, v93
	v_pk_fma_f32 v[14:15], v[14:15], v[74:75], v[94:95]
	s_waitcnt lgkmcnt(0)
	v_pk_mul_f32 v[30:31], v[10:11], v[74:75]
	v_mfma_f32_32x32x16_bf16 v[34:49], v[6:9], v[2:5], v[34:49]
	ds_read_b128 v[2:5], v213 offset:13312
	v_add_f32_e32 v98, v14, v28
	v_add_f32_e32 v99, v15, v29
	ds_read_b128 v[14:17], v213 offset:35840
	v_pk_mul_f32 v[26:27], v[12:13], v[76:77]
	s_waitcnt lgkmcnt(1)
	v_pk_mul_f32 v[4:5], v[4:5], v[80:81]
	v_pk_mul_f32 v[28:29], v[2:3], v[78:79]
	v_pk_fma_f32 v[2:3], v[12:13], v[76:77], v[4:5]
	v_pk_fma_f32 v[10:11], v[10:11], v[74:75], v[28:29]
	v_pk_add_f32 v[32:33], v[2:3], v[32:33]
	v_pk_add_f32 v[92:93], v[10:11], v[90:91]
	ds_read_b128 v[10:13], v213 offset:6144
	v_cvt_pk_bf16_f32 v5, v4, v5
	v_cvt_pk_bf16_f32 v3, v26, v27
	v_cvt_pk_bf16_f32 v4, v28, v29
	ds_read_b128 v[26:29], v213 offset:7168
	v_cvt_pk_bf16_f32 v2, v30, v31
	s_waitcnt lgkmcnt(1)
	v_pk_mul_f32 v[30:31], v[10:11], v[66:67]
	v_mfma_f32_32x32x16_bf16 v[50:65], v[6:9], v[2:5], v[50:65]
	v_mul_f32_e32 v2, v12, v68
	v_mul_f32_e32 v3, v13, v69
	s_waitcnt lgkmcnt(0)
	v_mul_f32_e32 v4, v28, v72
	v_mul_f32_e32 v5, v29, v73
	v_pk_mul_f32 v[6:7], v[26:27], v[70:71]
	v_pk_fma_f32 v[8:9], v[12:13], v[68:69], v[4:5]
	v_cvt_pk_bf16_f32 v3, v2, v3
	v_pk_fma_f32 v[10:11], v[10:11], v[66:67], v[6:7]
	v_pk_add_f32 v[94:95], v[8:9], v[96:97]
	v_cvt_pk_bf16_f32 v5, v4, v5
	v_cvt_pk_bf16_f32 v4, v6, v7
	ds_read_b128 v[6:9], v213 offset:14336
	v_pk_add_f32 v[96:97], v[10:11], v[98:99]
	ds_read_b128 v[10:13], v213 offset:15360
	v_cvt_pk_bf16_f32 v2, v30, v31
	s_waitcnt lgkmcnt(1)
	v_pk_mul_f32 v[30:31], v[6:7], v[66:67]
	v_mfma_f32_32x32x16_bf16 v[34:49], v[14:17], v[2:5], v[34:49]
	s_waitcnt lgkmcnt(0)
	v_mul_f32_e32 v10, v10, v70
	v_mul_f32_e32 v11, v11, v71
	v_mul_f32_e32 v2, v8, v68
	v_mul_f32_e32 v3, v9, v69
	v_pk_mul_f32 v[4:5], v[12:13], v[72:73]
	v_pk_fma_f32 v[6:7], v[6:7], v[66:67], v[10:11]
	v_pk_fma_f32 v[8:9], v[8:9], v[68:69], v[4:5]
	v_pk_add_f32 v[92:93], v[6:7], v[92:93]
	v_cvt_pk_bf16_f32 v3, v2, v3
	v_pk_add_f32 v[90:91], v[8:9], v[32:33]
	v_cvt_pk_bf16_f32 v5, v4, v5
	v_cvt_pk_bf16_f32 v4, v10, v11
	ds_read_b128 v[26:29], v213 offset:36864
	ds_read_b128 v[6:9], v213 offset:16384
	v_cvt_pk_bf16_f32 v2, v30, v31
	ds_read_b128 v[98:101], v213 offset:25600
	ds_read_b128 v[102:105], v213 offset:37888
	v_mfma_f32_32x32x16_bf16 v[50:65], v[14:17], v[2:5], v[50:65]
	ds_read_b128 v[2:5], v213 offset:17408
	ds_read_b128 v[30:33], v213 offset:24576
	s_waitcnt lgkmcnt(4)
	v_pk_mul_f32 v[12:13], v[6:7], v[18:19]
	v_pk_mul_f32 v[10:11], v[8:9], v[20:21]
	s_waitcnt lgkmcnt(1)
	v_pk_mul_f32 v[14:15], v[2:3], v[22:23]
	v_pk_mul_f32 v[22:23], v[98:99], v[22:23]
	v_pk_fma_f32 v[112:113], v[6:7], v[18:19], v[14:15]
	s_waitcnt lgkmcnt(0)
	v_pk_mul_f32 v[114:115], v[30:31], v[18:19]
	v_pk_fma_f32 v[118:119], v[30:31], v[18:19], v[22:23]
	v_pk_mul_f32 v[4:5], v[4:5], v[24:25]
	v_pk_mul_f32 v[106:107], v[32:33], v[20:21]
	v_pk_mul_f32 v[24:25], v[100:101], v[24:25]
	ds_read_b128 v[98:101], v213 offset:18432
	v_cvt_pk_bf16_f32 v19, v106, v107
	ds_read_b128 v[106:109], v213 offset:19456
	v_pk_fma_f32 v[110:111], v[8:9], v[20:21], v[4:5]
	v_cvt_pk_bf16_f32 v5, v4, v5
	v_cvt_pk_bf16_f32 v3, v10, v11
	v_cvt_pk_bf16_f32 v4, v14, v15
	s_waitcnt lgkmcnt(0)
	v_pk_mul_f32 v[106:107], v[106:107], v[86:87]
	v_cvt_pk_bf16_f32 v2, v12, v13
	v_pk_mul_f32 v[120:121], v[98:99], v[82:83]
	v_pk_mul_f32 v[108:109], v[108:109], v[88:89]
	v_pk_fma_f32 v[98:99], v[98:99], v[82:83], v[106:107]
	v_mfma_f32_32x32x16_bf16 v[2:17], v[26:29], v[2:5], 0
	v_cvt_pk_bf16_f32 v18, v114, v115
	v_mul_f32_e32 v114, v100, v84
	v_mul_f32_e32 v115, v101, v85
	v_fma_f32 v100, v100, v84, v108
	v_fma_f32 v101, v101, v85, v109
	v_pk_add_f32 v[124:125], v[98:99], v[112:113]
	v_pk_add_f32 v[122:123], v[100:101], v[110:111]
	v_cvt_pk_bf16_f32 v101, v108, v109
	v_cvt_pk_bf16_f32 v100, v106, v107
	ds_read_b128 v[106:109], v213 offset:26624
	v_pk_fma_f32 v[116:117], v[32:33], v[20:21], v[24:25]
	v_cvt_pk_bf16_f32 v21, v24, v25
	v_cvt_pk_bf16_f32 v20, v22, v23
	ds_read_b128 v[110:113], v213 offset:27648
	v_cvt_pk_bf16_f32 v99, v114, v115
	v_mfma_f32_32x32x16_bf16 v[18:33], v[26:29], v[18:21], 0
	v_cvt_pk_bf16_f32 v98, v120, v121
	s_waitcnt lgkmcnt(1)
	v_mul_f32_e32 v114, v106, v82
	v_mul_f32_e32 v115, v107, v83
	s_waitcnt lgkmcnt(0)
	v_pk_mul_f32 v[86:87], v[110:111], v[86:87]
	v_pk_mul_f32 v[88:89], v[112:113], v[88:89]
	v_pk_fma_f32 v[82:83], v[106:107], v[82:83], v[86:87]
	v_mfma_f32_32x32x16_bf16 v[2:17], v[102:105], v[98:101], v[2:17]
	v_mul_f32_e32 v98, v108, v84
	v_mul_f32_e32 v99, v109, v85
	v_fma_f32 v84, v108, v84, v88
	v_fma_f32 v85, v109, v85, v89
	v_add_f32_e32 v108, v82, v118
	v_add_f32_e32 v109, v83, v119
	v_cvt_pk_bf16_f32 v83, v98, v99
	v_pk_add_f32 v[106:107], v[84:85], v[116:117]
	v_cvt_pk_bf16_f32 v85, v88, v89
	v_cvt_pk_bf16_f32 v84, v86, v87
	ds_read_b128 v[86:89], v213 offset:38912
	ds_read_b128 v[98:101], v213 offset:20480
	v_cvt_pk_bf16_f32 v82, v114, v115
	s_waitcnt lgkmcnt(0)
	v_pk_mul_f32 v[110:111], v[100:101], v[76:77]
	v_mfma_f32_32x32x16_bf16 v[18:33], v[102:105], v[82:85], v[18:33]
	ds_read_b128 v[82:85], v213 offset:21504
	ds_read_b128 v[102:105], v213 offset:28672
	v_mul_f32_e32 v112, v98, v74
	v_mul_f32_e32 v113, v99, v75
	s_waitcnt lgkmcnt(1)
	v_pk_mul_f32 v[84:85], v[84:85], v[80:81]
	v_pk_mul_f32 v[114:115], v[82:83], v[78:79]
	v_pk_fma_f32 v[82:83], v[100:101], v[76:77], v[84:85]
	v_cvt_pk_bf16_f32 v85, v84, v85
	v_pk_add_f32 v[116:117], v[82:83], v[122:123]
	v_cvt_pk_bf16_f32 v83, v110, v111
	v_cvt_pk_bf16_f32 v84, v114, v115
	v_cvt_pk_bf16_f32 v82, v112, v113
	v_pk_fma_f32 v[98:99], v[98:99], v[74:75], v[114:115]
	s_waitcnt lgkmcnt(0)
	v_pk_mul_f32 v[112:113], v[102:103], v[74:75]
	v_mfma_f32_32x32x16_bf16 v[2:17], v[86:89], v[82:85], v[2:17]
	ds_read_b128 v[82:85], v213 offset:29696
	v_add_f32_e32 v118, v98, v124
	v_add_f32_e32 v119, v99, v125
	v_mul_f32_e32 v110, v104, v76
	v_mul_f32_e32 v111, v105, v77
	ds_read_b128 v[98:101], v213 offset:39936
	s_waitcnt lgkmcnt(1)
	v_pk_mul_f32 v[78:79], v[82:83], v[78:79]
	v_pk_mul_f32 v[80:81], v[84:85], v[80:81]
	v_pk_fma_f32 v[74:75], v[102:103], v[74:75], v[78:79]
	v_pk_fma_f32 v[76:77], v[104:105], v[76:77], v[80:81]
	v_pk_add_f32 v[104:105], v[74:75], v[108:109]
	v_pk_add_f32 v[102:103], v[76:77], v[106:107]
	v_cvt_pk_bf16_f32 v77, v80, v81
	v_cvt_pk_bf16_f32 v76, v78, v79
	ds_read_b128 v[78:81], v213 offset:22528
	ds_read_b128 v[82:85], v213 offset:23552
	v_cvt_pk_bf16_f32 v75, v110, v111
	v_cvt_pk_bf16_f32 v74, v112, v113
	s_waitcnt lgkmcnt(0)
	v_pk_mul_f32 v[82:83], v[82:83], v[70:71]
	v_mfma_f32_32x32x16_bf16 v[18:33], v[86:89], v[74:77], v[18:33]
	v_mul_f32_e32 v74, v80, v68
	v_mul_f32_e32 v75, v81, v69
	v_mul_f32_e32 v76, v84, v72
	v_mul_f32_e32 v77, v85, v73
	v_mul_f32_e32 v86, v78, v66
	v_mul_f32_e32 v87, v79, v67
	v_pk_fma_f32 v[80:81], v[80:81], v[68:69], v[76:77]
	v_pk_fma_f32 v[78:79], v[78:79], v[66:67], v[82:83]
	v_cvt_pk_bf16_f32 v75, v74, v75
	v_pk_add_f32 v[88:89], v[80:81], v[116:117]
	v_pk_add_f32 v[106:107], v[78:79], v[118:119]
	ds_read_b128 v[78:81], v213 offset:30720
	v_cvt_pk_bf16_f32 v77, v76, v77
	v_cvt_pk_bf16_f32 v76, v82, v83
	ds_read_b128 v[82:85], v213 offset:31744
	v_cvt_pk_bf16_f32 v74, v86, v87
	s_waitcnt lgkmcnt(0)
	v_pk_mul_f32 v[72:73], v[84:85], v[72:73]
	v_mfma_f32_32x32x16_bf16 v[2:17], v[98:101], v[74:77], v[2:17]
	v_mul_f32_e32 v74, v80, v68
	v_mul_f32_e32 v75, v81, v69
	v_fma_f32 v68, v80, v68, v72
	v_fma_f32 v69, v81, v69, v73
	v_mul_f32_e32 v70, v82, v70
	v_mul_f32_e32 v71, v83, v71
	v_pk_add_f32 v[84:85], v[68:69], v[102:103]
	v_cvt_pk_bf16_f32 v69, v72, v73
	v_pk_mov_b32 v[72:73], v[96:97], v[94:95] op_sel:[1,0]
	v_mov_b32_e32 v97, v95
	v_pk_add_f32 v[72:73], v[72:73], v[96:97]
	v_pk_mul_f32 v[76:77], v[78:79], v[66:67]
	v_pk_fma_f32 v[66:67], v[78:79], v[66:67], v[70:71]
	v_pk_add_f32 v[72:73], v[72:73], v[72:73] op_sel:[0,1] op_sel_hi:[1,0]
	v_pk_add_f32 v[86:87], v[66:67], v[104:105]
	v_mov_b32_e32 v66, v72
	s_nop 1
	v_permlane32_swap_b32_e32 v72, v66
	v_add_f32_e32 v66, v72, v66
	v_cvt_pk_bf16_f32 v67, v74, v75
	v_rcp_f32_e32 v74, v66
	v_cvt_pk_bf16_f32 v68, v70, v71
	v_cvt_pk_bf16_f32 v66, v76, v77
	v_pk_mul_f32 v[70:71], v[46:47], v[74:75] op_sel_hi:[1,0]
	s_nop 0
	v_mfma_f32_32x32x16_bf16 v[18:33], v[98:101], v[66:69], v[18:33]
	v_mul_f32_e32 v66, v42, v74
	v_mul_f32_e32 v67, v43, v74
	v_pk_mov_b32 v[42:43], v[92:93], v[90:91] op_sel:[1,0]
	v_mov_b32_e32 v93, v91
	v_pk_add_f32 v[42:43], v[42:43], v[92:93]
	v_pk_mul_f32 v[68:69], v[44:45], v[74:75] op_sel_hi:[1,0]
	v_pk_add_f32 v[42:43], v[42:43], v[42:43] op_sel:[0,1] op_sel_hi:[1,0]
	v_pk_mov_b32 v[44:45], v[106:107], v[88:89] op_sel:[1,0]
	v_mov_b32_e32 v43, v42
	s_nop 1
	v_permlane32_swap_b32_e32 v42, v43
	v_add_f32_e32 v42, v42, v43
	v_rcp_f32_e32 v42, v42
	v_mov_b32_e32 v107, v89
	v_pk_add_f32 v[44:45], v[44:45], v[106:107]
	v_pk_mul_f32 v[72:73], v[48:49], v[74:75] op_sel_hi:[1,0]
	v_pk_add_f32 v[44:45], v[44:45], v[44:45] op_sel:[0,1] op_sel_hi:[1,0]
	v_pk_mul_f32 v[36:37], v[36:37], v[74:75] op_sel_hi:[1,0]
	v_pk_mul_f32 v[38:39], v[38:39], v[74:75] op_sel_hi:[1,0]
	v_pk_mul_f32 v[40:41], v[40:41], v[74:75] op_sel_hi:[1,0]
	v_pk_mul_f32 v[34:35], v[34:35], v[74:75] op_sel_hi:[1,0]
	v_pk_mul_f32 v[74:75], v[58:59], v[42:43] op_sel_hi:[1,0]
	v_pk_mul_f32 v[78:79], v[60:61], v[42:43] op_sel_hi:[1,0]
	v_pk_mul_f32 v[80:81], v[62:63], v[42:43] op_sel_hi:[1,0]
	v_pk_mul_f32 v[82:83], v[64:65], v[42:43] op_sel_hi:[1,0]
	v_pk_mul_f32 v[92:93], v[52:53], v[42:43] op_sel_hi:[1,0]
	v_mov_b32_e32 v43, v44
	s_nop 1
	v_permlane32_swap_b32_e32 v44, v43
	v_add_f32_e32 v43, v44, v43
	v_rcp_f32_e32 v76, v43
	v_pk_mul_f32 v[96:97], v[54:55], v[42:43] op_sel_hi:[1,0]
	v_pk_mul_f32 v[94:95], v[56:57], v[42:43] op_sel_hi:[1,0]
	v_pk_mul_f32 v[98:99], v[50:51], v[42:43] op_sel_hi:[1,0]
	v_pk_mul_f32 v[100:101], v[4:5], v[76:77] op_sel_hi:[1,0]
	v_pk_mov_b32 v[4:5], v[86:87], v[84:85] op_sel:[1,0]
	v_mov_b32_e32 v87, v85
	v_pk_add_f32 v[4:5], v[4:5], v[86:87]
	v_pk_mul_f32 v[102:103], v[6:7], v[76:77] op_sel_hi:[1,0]
	v_pk_add_f32 v[104:105], v[4:5], v[4:5] op_sel:[0,1] op_sel_hi:[1,0]
	v_cvt_pk_bf16_f32 v7, v40, v41
	ds_read_b128 v[84:87], v150 offset:52224
	ds_read_b128 v[50:53], v150 offset:35840
	ds_read_b128 v[54:57], v150 offset:36864
	ds_read_b128 v[58:61], v150 offset:37888
	ds_read_b128 v[62:65], v150 offset:38912
	v_cvt_pk_bf16_f32 v6, v38, v39
	v_cvt_pk_bf16_f32 v5, v36, v37
	v_cvt_pk_bf16_f32 v4, v34, v35
	ds_read_b128 v[88:91], v150 offset:53248
	ds_read_b128 v[34:37], v150 offset:39936
	ds_read_b128 v[38:41], v150 offset:40960
	ds_read_b128 v[42:45], v150 offset:41984
	ds_read_b128 v[46:49], v150 offset:43008
	v_cvt_pk_bf16_f32 v95, v94, v95
	v_cvt_pk_bf16_f32 v94, v96, v97
	v_cvt_pk_bf16_f32 v93, v92, v93
	v_cvt_pk_bf16_f32 v92, v98, v99
	s_waitcnt lgkmcnt(5)
	v_mfma_f32_32x32x16_bf16 v[50:65], v[84:87], v[4:7], v[50:65]
	v_mul_f32_e32 v10, v10, v76
	v_mul_f32_e32 v11, v11, v76
	v_mul_f32_e32 v12, v12, v76
	v_mul_f32_e32 v13, v13, v76
	v_mul_f32_e32 v8, v8, v76
	v_mul_f32_e32 v9, v9, v76
	v_mov_b32_e32 v77, v104
	s_nop 1
	v_permlane32_swap_b32_e32 v104, v77
	v_cvt_pk_bf16_f32 v73, v72, v73
	s_waitcnt lgkmcnt(0)
	v_mfma_f32_32x32x16_bf16 v[34:49], v[84:87], v[92:95], v[34:49]
	v_cvt_pk_bf16_f32 v72, v70, v71
	v_cvt_pk_bf16_f32 v70, v66, v67
	v_add_f32_e32 v66, v104, v77
	v_cvt_pk_bf16_f32 v71, v68, v69
	v_rcp_f32_e32 v104, v66
	v_cvt_pk_bf16_f32 v69, v82, v83
	v_cvt_pk_bf16_f32 v68, v80, v81
	v_cvt_pk_bf16_f32 v67, v78, v79
	v_cvt_pk_bf16_f32 v66, v74, v75
	ds_read_b128 v[78:81], v150 offset:54272
	v_mfma_f32_32x32x16_bf16 v[50:65], v[88:91], v[70:73], v[50:65]
	v_mul_f32_e32 v2, v2, v76
	v_mul_f32_e32 v3, v3, v76
	v_mul_f32_e32 v20, v20, v104
	v_mul_f32_e32 v21, v21, v104
	v_cvt_pk_bf16_f32 v85, v8, v9
	v_cvt_pk_bf16_f32 v82, v2, v3
	v_pk_mul_f32 v[2:3], v[22:23], v[104:105] op_sel_hi:[1,0]
	v_pk_mul_f32 v[8:9], v[24:25], v[104:105] op_sel_hi:[1,0]
	v_pk_mul_f32 v[18:19], v[18:19], v[104:105] op_sel_hi:[1,0]
	v_mfma_f32_32x32x16_bf16 v[34:49], v[88:91], v[66:69], v[34:49]
	v_cvt_pk_bf16_f32 v84, v102, v103
	v_cvt_pk_bf16_f32 v83, v100, v101
	ds_read_b128 v[86:89], v150 offset:55296
	v_cvt_pk_bf16_f32 v99, v8, v9
	v_cvt_pk_bf16_f32 v98, v2, v3
	v_cvt_pk_bf16_f32 v97, v20, v21
	v_cvt_pk_bf16_f32 v96, v18, v19
	s_waitcnt lgkmcnt(1)
	v_mfma_f32_32x32x16_bf16 v[50:65], v[78:81], v[82:85], v[50:65]
	v_mul_f32_e32 v2, v14, v76
	v_mul_f32_e32 v3, v15, v76
	v_mul_f32_e32 v8, v16, v76
	v_mul_f32_e32 v9, v17, v76
	v_mul_f32_e32 v14, v26, v104
	v_mul_f32_e32 v15, v27, v104
	v_cvt_pk_bf16_f32 v77, v8, v9
	v_cvt_pk_bf16_f32 v76, v2, v3
	v_cvt_pk_bf16_f32 v74, v10, v11
	v_pk_mul_f32 v[2:3], v[28:29], v[104:105] op_sel_hi:[1,0]
	v_mfma_f32_32x32x16_bf16 v[34:49], v[78:81], v[96:99], v[34:49]
	v_mul_f32_e32 v8, v30, v104
	v_mul_f32_e32 v9, v31, v104
	v_mul_f32_e32 v10, v32, v104
	v_mul_f32_e32 v11, v33, v104
	v_cvt_pk_bf16_f32 v75, v12, v13
	v_cvt_pk_bf16_f32 v81, v10, v11
	v_cvt_pk_bf16_f32 v80, v8, v9
	v_cvt_pk_bf16_f32 v79, v2, v3
	v_cvt_pk_bf16_f32 v78, v14, v15
	s_waitcnt lgkmcnt(0)
	v_mfma_f32_32x32x16_bf16 v[50:65], v[86:89], v[74:77], v[50:65]
	v_mfma_f32_32x32x16_bf16 v[34:49], v[86:89], v[78:81], v[34:49]
	ds_read_b128 v[86:89], v150 offset:56320
	ds_read_b128 v[18:21], v150 offset:44032
	ds_read_b128 v[22:25], v150 offset:45056
	ds_read_b128 v[26:29], v150 offset:46080
	ds_read_b128 v[30:33], v150 offset:47104
	ds_read_b128 v[100:103], v150 offset:57344
	s_waitcnt lgkmcnt(1)
	v_mfma_f32_32x32x16_bf16 v[18:33], v[86:89], v[4:7], v[18:33]
	ds_read_b128 v[2:5], v150 offset:48128
	ds_read_b128 v[6:9], v150 offset:49152
	ds_read_b128 v[10:13], v150 offset:50176
	ds_read_b128 v[14:17], v150 offset:51200
	s_waitcnt lgkmcnt(0)
	v_mfma_f32_32x32x16_bf16 v[2:17], v[86:89], v[92:95], v[2:17]
	v_mfma_f32_32x32x16_bf16 v[18:33], v[100:103], v[70:73], v[18:33]
	v_mfma_f32_32x32x16_bf16 v[2:17], v[100:103], v[66:69], v[2:17]
	ds_read_b128 v[66:69], v150 offset:58368
	ds_read_b128 v[70:73], v150 offset:59392
	s_waitcnt lgkmcnt(1)
	v_mfma_f32_32x32x16_bf16 v[18:33], v[66:69], v[82:85], v[18:33]
	v_mfma_f32_32x32x16_bf16 v[2:17], v[66:69], v[96:99], v[2:17]
	s_waitcnt lgkmcnt(0)
	v_mfma_f32_32x32x16_bf16 v[18:33], v[70:73], v[74:77], v[18:33]
	v_mfma_f32_32x32x16_bf16 v[2:17], v[70:73], v[78:81], v[2:17]
	s_nop 10
	v_mul_f32_e32 v66, v22, v22
	v_mul_f32_e32 v67, v23, v23
	v_mul_f32_e32 v68, v30, v30
	v_mul_f32_e32 v69, v31, v31
	v_mul_f32_e32 v70, v24, v24
	v_mul_f32_e32 v71, v25, v25
	v_pk_mul_f32 v[72:73], v[32:33], v[32:33]
	v_pk_mul_f32 v[74:75], v[20:21], v[20:21]
	v_pk_mul_f32 v[76:77], v[28:29], v[28:29]
	v_pk_mul_f32 v[78:79], v[26:27], v[26:27]
	v_pk_mul_f32 v[80:81], v[18:19], v[18:19]
	v_pk_fma_f32 v[78:79], v[58:59], v[58:59], v[78:79]
	v_pk_fma_f32 v[76:77], v[60:61], v[60:61], v[76:77]
	v_pk_fma_f32 v[74:75], v[52:53], v[52:53], v[74:75]
	v_pk_fma_f32 v[72:73], v[64:65], v[64:65], v[72:73]
	v_pk_fma_f32 v[70:71], v[56:57], v[56:57], v[70:71]
	v_pk_fma_f32 v[68:69], v[62:63], v[62:63], v[68:69]
	v_pk_fma_f32 v[66:67], v[54:55], v[54:55], v[66:67]
	v_pk_fma_f32 v[80:81], v[50:51], v[50:51], v[80:81]
	v_pk_add_f32 v[66:67], v[66:67], v[68:69]
	v_pk_add_f32 v[68:69], v[70:71], v[72:73]
	v_pk_add_f32 v[70:71], v[74:75], v[76:77]
	v_pk_add_f32 v[72:73], v[80:81], v[78:79]
	v_pk_add_f32 v[68:69], v[70:71], v[68:69]
	v_pk_add_f32 v[66:67], v[72:73], v[66:67]
	v_pk_mul_f32 v[72:73], v[14:15], v[14:15]
	v_pk_mov_b32 v[70:71], v[66:67], v[68:69] op_sel:[1,0]
	v_mov_b32_e32 v67, v69
	v_pk_add_f32 v[66:67], v[70:71], v[66:67]
	v_pk_mul_f32 v[70:71], v[6:7], v[6:7]
	v_pk_mul_f32 v[74:75], v[8:9], v[8:9]
	v_pk_mul_f32 v[76:77], v[16:17], v[16:17]
	v_pk_mul_f32 v[78:79], v[4:5], v[4:5]
	v_pk_mul_f32 v[80:81], v[12:13], v[12:13]
	v_pk_mul_f32 v[82:83], v[10:11], v[10:11]
	v_pk_mul_f32 v[84:85], v[2:3], v[2:3]
	v_pk_fma_f32 v[82:83], v[42:43], v[42:43], v[82:83]
	v_pk_fma_f32 v[80:81], v[44:45], v[44:45], v[80:81]
	v_pk_fma_f32 v[78:79], v[36:37], v[36:37], v[78:79]
	v_pk_fma_f32 v[76:77], v[48:49], v[48:49], v[76:77]
	v_pk_fma_f32 v[74:75], v[40:41], v[40:41], v[74:75]
	v_pk_fma_f32 v[72:73], v[46:47], v[46:47], v[72:73]
	v_pk_fma_f32 v[70:71], v[38:39], v[38:39], v[70:71]
	v_pk_fma_f32 v[84:85], v[34:35], v[34:35], v[84:85]
	v_pk_add_f32 v[70:71], v[70:71], v[72:73]
	v_pk_add_f32 v[72:73], v[74:75], v[76:77]
	v_pk_add_f32 v[74:75], v[78:79], v[80:81]
	v_pk_add_f32 v[76:77], v[84:85], v[82:83]
	v_pk_add_f32 v[72:73], v[74:75], v[72:73]
	v_pk_add_f32 v[70:71], v[76:77], v[70:71]
	v_pk_add_f32 v[66:67], v[66:67], v[66:67] op_sel:[0,1] op_sel_hi:[1,0]
	v_pk_mov_b32 v[74:75], v[70:71], v[72:73] op_sel:[1,0]
	v_mov_b32_e32 v71, v73
	v_pk_add_f32 v[70:71], v[74:75], v[70:71]
	v_mov_b32_e32 v69, v66
	v_pk_add_f32 v[70:71], v[70:71], v[70:71] op_sel:[0,1] op_sel_hi:[1,0]
	s_nop 0
	v_permlane32_swap_b32_e32 v66, v69
	v_mov_b32_e32 v68, v70
	s_nop 1
	v_permlane32_swap_b32_e32 v70, v68
	v_mov_b32_e32 v71, v66
	v_pk_add_f32 v[66:67], v[70:71], v[68:69]
	v_pk_fma_f32 v[66:67], v[66:67], s[0:1], v[152:153] op_sel_hi:[1,0,0]
	s_mov_b32 s1, 0x800000
	v_mul_f32_e32 v68, 0x4b800000, v67
	v_cmp_gt_f32_e32 vcc, s1, v67
	s_nop 1
	v_cndmask_b32_e32 v67, v67, v68, vcc
	v_rsq_f32_e32 v67, v67
	s_nop 0
	v_mul_f32_e32 v68, 0x45800000, v67
	v_cndmask_b32_e32 v68, v67, v68, vcc
	v_pk_mul_f32 v[158:159], v[50:51], v[68:69] op_sel_hi:[1,0]
	v_pk_mul_f32 v[50:51], v[18:19], v[68:69] op_sel_hi:[1,0]
	v_mul_f32_e32 v18, 0x4b800000, v66
	v_cmp_gt_f32_e32 vcc, s1, v66
	v_pk_mul_f32 v[80:81], v[60:61], v[68:69] op_sel_hi:[1,0]
	v_pk_mul_f32 v[60:61], v[28:29], v[68:69] op_sel_hi:[1,0]
	v_cndmask_b32_e32 v18, v66, v18, vcc
	v_rsq_f32_e32 v18, v18
	v_pk_mul_f32 v[78:79], v[58:59], v[68:69] op_sel_hi:[1,0]
	v_pk_mul_f32 v[160:161], v[52:53], v[68:69] op_sel_hi:[1,0]
	v_pk_mul_f32 v[82:83], v[54:55], v[68:69] op_sel_hi:[1,0]
	v_mul_f32_e32 v19, 0x45800000, v18
	v_cndmask_b32_e32 v28, v18, v19, vcc
	v_pk_mul_f32 v[168:169], v[56:57], v[68:69] op_sel_hi:[1,0]
	v_pk_mul_f32 v[58:59], v[26:27], v[68:69] op_sel_hi:[1,0]
	v_pk_mul_f32 v[52:53], v[20:21], v[68:69] op_sel_hi:[1,0]
	v_pk_mul_f32 v[54:55], v[22:23], v[68:69] op_sel_hi:[1,0]
	v_pk_mul_f32 v[56:57], v[24:25], v[68:69] op_sel_hi:[1,0]
	v_pk_mul_f32 v[18:19], v[42:43], v[28:29] op_sel_hi:[1,0]
	v_pk_mul_f32 v[20:21], v[44:45], v[28:29] op_sel_hi:[1,0]
	v_pk_mul_f32 v[22:23], v[46:47], v[28:29] op_sel_hi:[1,0]
	v_pk_mul_f32 v[26:27], v[48:49], v[28:29] op_sel_hi:[1,0]
	v_pk_mul_f32 v[162:163], v[34:35], v[28:29] op_sel_hi:[1,0]
	v_pk_mul_f32 v[164:165], v[36:37], v[28:29] op_sel_hi:[1,0]
	v_pk_mul_f32 v[166:167], v[38:39], v[28:29] op_sel_hi:[1,0]
	v_pk_mul_f32 v[24:25], v[40:41], v[28:29] op_sel_hi:[1,0]
	v_pk_mul_f32 v[104:105], v[2:3], v[28:29] op_sel_hi:[1,0]
	v_pk_mul_f32 v[112:113], v[4:5], v[28:29] op_sel_hi:[1,0]
	ds_read_b128 v[2:5], v150 offset:60416
	ds_read_b128 v[34:37], v174 offset:32768
	ds_read_b128 v[38:41], v174 offset:32800
	ds_read_b128 v[42:45], v174 offset:32832
	ds_read_b128 v[46:49], v174 offset:32864
	v_cvt_pk_bf16_f32 v129, v168, v169
	v_cvt_pk_bf16_f32 v128, v82, v83
	v_cvt_pk_bf16_f32 v127, v160, v161
	v_cvt_pk_bf16_f32 v126, v158, v159
	v_cvt_pk_bf16_f32 v137, v24, v25
	v_cvt_pk_bf16_f32 v136, v166, v167
	v_cvt_pk_bf16_f32 v135, v164, v165
	s_waitcnt lgkmcnt(0)
	v_mfma_f32_32x32x16_bf16 v[86:101], v[2:5], v[126:129], v[34:49]
	v_cvt_pk_bf16_f32 v134, v162, v163
	v_mul_f32_e32 v84, v62, v68
	v_mul_f32_e32 v85, v63, v68
	v_mul_f32_e32 v170, v64, v68
	v_mul_f32_e32 v171, v65, v68
	v_pk_mul_f32 v[62:63], v[30:31], v[68:69] op_sel_hi:[1,0]
	v_pk_mul_f32 v[64:65], v[32:33], v[68:69] op_sel_hi:[1,0]
	v_pk_mul_f32 v[116:117], v[6:7], v[28:29] op_sel_hi:[1,0]
	v_pk_mul_f32 v[154:155], v[8:9], v[28:29] op_sel_hi:[1,0]
	v_mfma_f32_32x32x16_bf16 v[34:49], v[2:5], v[134:137], v[34:49]
	ds_read_b128 v[6:9], v150 offset:61440
	ds_read_b128 v[66:69], v174 offset:32896
	ds_read_b128 v[106:109], v150 offset:64512
	v_cvt_pk_bf16_f32 v125, v170, v171
	v_cvt_pk_bf16_f32 v124, v84, v85
	v_cvt_pk_bf16_f32 v123, v80, v81
	v_cvt_pk_bf16_f32 v122, v78, v79
	v_cvt_pk_bf16_f32 v149, v26, v27
	v_cvt_pk_bf16_f32 v148, v22, v23
	v_cvt_pk_bf16_f32 v147, v20, v21
	v_cvt_pk_bf16_f32 v146, v18, v19
	s_waitcnt lgkmcnt(2)
	v_mfma_f32_32x32x16_bf16 v[86:101], v[6:9], v[122:125], v[86:101]
	v_mul_f32_e32 v102, v10, v28
	v_mul_f32_e32 v103, v11, v28
	v_mul_f32_e32 v110, v12, v28
	v_mul_f32_e32 v111, v13, v28
	v_mul_f32_e32 v114, v14, v28
	v_mul_f32_e32 v115, v15, v28
	v_pk_mul_f32 v[156:157], v[16:17], v[28:29] op_sel_hi:[1,0]
	ds_read_b128 v[176:179], v174 offset:33536
	ds_read_b128 v[180:183], v174 offset:33568
	ds_read_b128 v[184:187], v174 offset:33600
	ds_read_b128 v[28:31], v174 offset:33632
	ds_read_b128 v[188:191], v174 offset:33792
	ds_read_b128 v[192:195], v174 offset:33824
	ds_read_b128 v[196:199], v174 offset:33856
	ds_read_b128 v[200:203], v174 offset:33888
	ds_read_b128 v[204:207], v150 offset:62464
	v_cvt_pk_bf16_f32 v133, v56, v57
	v_mfma_f32_32x32x16_bf16 v[34:49], v[6:9], v[146:149], v[34:49]
	v_cvt_pk_bf16_f32 v132, v54, v55
	v_cvt_pk_bf16_f32 v131, v52, v53
	v_cvt_pk_bf16_f32 v130, v50, v51
	ds_read_b128 v[70:73], v174 offset:33664
	ds_read_b128 v[74:77], v174 offset:33920
	ds_read_b128 v[208:211], v150 offset:63488
	v_cvt_pk_bf16_f32 v145, v154, v155
	v_cvt_pk_bf16_f32 v144, v116, v117
	v_cvt_pk_bf16_f32 v143, v112, v113
	v_cvt_pk_bf16_f32 v142, v104, v105
	s_waitcnt lgkmcnt(3)
	v_mfma_f32_32x32x16_bf16 v[86:101], v[204:207], v[130:133], v[86:101]
	v_cvt_pk_bf16_f32 v121, v64, v65
	v_cvt_pk_bf16_f32 v120, v62, v63
	v_cvt_pk_bf16_f32 v119, v60, v61
	v_cvt_pk_bf16_f32 v118, v58, v59
	v_cvt_pk_bf16_f32 v141, v156, v157
	v_cvt_pk_bf16_f32 v140, v114, v115
	v_cvt_pk_bf16_f32 v139, v110, v111
	v_mfma_f32_32x32x16_bf16 v[34:49], v[204:207], v[142:145], v[34:49]
	v_cvt_pk_bf16_f32 v138, v102, v103
	v_fma_f32 v16, v30, v170, v202
	v_fma_f32 v17, v31, v171, v203
	v_fma_f32 v14, v28, v84, v200
	v_fma_f32 v15, v29, v85, v201
	v_pk_fma_f32 v[12:13], v[186:187], v[80:81], v[198:199]
	v_pk_fma_f32 v[10:11], v[184:185], v[78:79], v[196:197]
	v_pk_fma_f32 v[8:9], v[182:183], v[168:169], v[194:195]
	s_waitcnt lgkmcnt(0)
	v_mfma_f32_32x32x16_bf16 v[86:101], v[208:211], v[118:121], v[86:101]
	v_fma_f32 v6, v180, v82, v192
	v_fma_f32 v7, v181, v83, v193
	ds_read_b128 v[78:81], v174 offset:33760
	ds_read_b128 v[82:85], v174 offset:33248
	v_fma_f32 v4, v178, v160, v190
	v_fma_f32 v5, v179, v161, v191
	v_pk_fma_f32 v[2:3], v[176:177], v[158:159], v[188:189]
	v_pk_fma_f32 v[32:33], v[30:31], v[26:27], v[202:203]
	v_pk_fma_f32 v[30:31], v[28:29], v[22:23], v[200:201]
	v_pk_fma_f32 v[28:29], v[186:187], v[20:21], v[198:199]
	v_pk_fma_f32 v[26:27], v[184:185], v[18:19], v[196:197]
	v_pk_fma_f32 v[24:25], v[182:183], v[24:25], v[194:195]
	v_pk_fma_f32 v[22:23], v[180:181], v[166:167], v[192:193]
	v_pk_fma_f32 v[20:21], v[178:179], v[164:165], v[190:191]
	v_pk_fma_f32 v[18:19], v[176:177], v[162:163], v[188:189]
	ds_read_b128 v[158:161], v174 offset:33696
	ds_read_b128 v[162:165], v174 offset:33728
	ds_read_b128 v[166:169], v174 offset:33952
	ds_read_b128 v[176:179], v174 offset:33984
	ds_read_b128 v[180:183], v174 offset:34016
	ds_read_b128 v[184:187], v212 offset:11264
	v_mfma_f32_32x32x16_bf16 v[34:49], v[208:211], v[138:141], v[34:49]
	v_cvt_pk_bf16_f32 v86, v86, v87
	v_cvt_pk_bf16_f32 v87, v88, v89
	v_cvt_pk_bf16_f32 v88, v90, v91
	v_cvt_pk_bf16_f32 v89, v92, v93
	ds_read_b128 v[90:93], v212 offset:12288
	v_pk_max_i16 v86, v86, 0
	v_pk_max_i16 v87, v87, 0
	v_pk_max_i16 v88, v88, 0
	v_pk_max_i16 v89, v89, 0
	s_nop 1
	s_nop 0
	v_cvt_pk_bf16_f32 v188, v34, v35
	v_cvt_pk_bf16_f32 v189, v36, v37
	v_cvt_pk_bf16_f32 v190, v38, v39
	v_cvt_pk_bf16_f32 v191, v40, v41
	s_waitcnt lgkmcnt(1)
	v_mfma_f32_32x32x16_bf16 v[2:17], v[184:187], v[86:89], v[2:17]
	v_pk_max_i16 v188, v188, 0
	v_pk_max_i16 v189, v189, 0
	v_pk_max_i16 v190, v190, 0
	v_pk_max_i16 v191, v191, 0
	v_cvt_pk_bf16_f32 v94, v94, v95
	v_cvt_pk_bf16_f32 v95, v96, v97
	v_cvt_pk_bf16_f32 v96, v98, v99
	v_cvt_pk_bf16_f32 v97, v100, v101
	v_cvt_pk_bf16_f32 v98, v42, v43
	v_cvt_pk_bf16_f32 v99, v44, v45
	v_mfma_f32_32x32x16_bf16 v[18:33], v[184:187], v[188:191], v[18:33]
	ds_read_b128 v[184:187], v212 offset:19456
	v_cvt_pk_bf16_f32 v100, v46, v47
	v_cvt_pk_bf16_f32 v101, v48, v49
	v_fma_f32 v64, v80, v64, v182
	v_fma_f32 v65, v81, v65, v183
	v_pk_fma_f32 v[62:63], v[78:79], v[62:63], v[180:181]
	v_pk_fma_f32 v[60:61], v[164:165], v[60:61], v[178:179]
	v_pk_fma_f32 v[58:59], v[162:163], v[58:59], v[176:177]
	v_pk_max_i16 v94, v94, 0
	v_pk_max_i16 v95, v95, 0
	v_pk_max_i16 v96, v96, 0
	v_pk_max_i16 v97, v97, 0
	v_pk_max_i16 v98, v98, 0
	v_pk_max_i16 v99, v99, 0
	v_pk_max_i16 v100, v100, 0
	v_pk_max_i16 v101, v101, 0
	v_pk_fma_f32 v[56:57], v[160:161], v[56:57], v[168:169]
	s_waitcnt lgkmcnt(1)
	v_mfma_f32_32x32x16_bf16 v[2:17], v[90:93], v[94:97], v[2:17]
	v_fma_f32 v54, v158, v54, v166
	v_fma_f32 v55, v159, v55, v167
	v_fma_f32 v52, v72, v52, v76
	v_fma_f32 v53, v73, v53, v77
	v_fma_f32 v50, v70, v50, v74
	v_fma_f32 v51, v71, v51, v75
	v_pk_fma_f32 v[48:49], v[80:81], v[156:157], v[182:183]
	v_pk_fma_f32 v[46:47], v[78:79], v[114:115], v[180:181]
	v_pk_fma_f32 v[44:45], v[164:165], v[110:111], v[178:179]
	v_pk_fma_f32 v[42:43], v[162:163], v[102:103], v[176:177]
	v_mfma_f32_32x32x16_bf16 v[18:33], v[90:93], v[98:101], v[18:33]
	ds_read_b128 v[90:93], v212 offset:20480
	v_fma_f32 v40, v160, v154, v168
	v_fma_f32 v41, v161, v155, v169
	v_fma_f32 v38, v158, v116, v166
	v_fma_f32 v39, v159, v117, v167
	v_pk_fma_f32 v[36:37], v[72:73], v[112:113], v[76:77]
	v_pk_fma_f32 v[34:35], v[70:71], v[104:105], v[74:75]
	s_waitcnt lgkmcnt(1)
	v_mfma_f32_32x32x16_bf16 v[50:65], v[184:187], v[86:89], v[50:65]
	ds_read_b128 v[70:73], v174 offset:32928
	ds_read_b128 v[74:77], v174 offset:32960
	ds_read_b128 v[78:81], v174 offset:32992
	ds_read_b128 v[86:89], v174 offset:33024
	ds_read_b128 v[110:113], v212 offset:1024
	v_mfma_f32_32x32x16_bf16 v[34:49], v[184:187], v[188:191], v[34:49]
	s_waitcnt lgkmcnt(5)
	v_mfma_f32_32x32x16_bf16 v[50:65], v[90:93], v[94:97], v[50:65]
	v_mfma_f32_32x32x16_bf16 v[34:49], v[90:93], v[98:101], v[34:49]
	s_waitcnt lgkmcnt(2)
	v_mfma_f32_32x32x16_bf16 v[90:105], v[106:109], v[126:129], v[66:81]
	v_mfma_f32_32x32x16_bf16 v[66:81], v[106:109], v[134:137], v[66:81]
	ds_read_b128 v[106:109], v212 offset:0
	s_waitcnt lgkmcnt(0)
	v_mfma_f32_32x32x16_bf16 v[90:105], v[106:109], v[122:125], v[90:105]
	v_mfma_f32_32x32x16_bf16 v[66:81], v[106:109], v[146:149], v[66:81]
	ds_read_b128 v[106:109], v212 offset:2048
	v_mfma_f32_32x32x16_bf16 v[90:105], v[110:113], v[130:133], v[90:105]
	v_mfma_f32_32x32x16_bf16 v[66:81], v[110:113], v[142:145], v[66:81]
	ds_read_b128 v[110:113], v212 offset:13312
	s_waitcnt lgkmcnt(1)
	v_mfma_f32_32x32x16_bf16 v[90:105], v[106:109], v[118:121], v[90:105]
	v_mfma_f32_32x32x16_bf16 v[66:81], v[106:109], v[138:141], v[66:81]
	s_nop 10
	v_cvt_pk_bf16_f32 v90, v90, v91
	v_cvt_pk_bf16_f32 v91, v92, v93
	v_cvt_pk_bf16_f32 v92, v94, v95
	v_cvt_pk_bf16_f32 v94, v98, v99
	v_cvt_pk_bf16_f32 v95, v100, v101
	ds_read_b128 v[98:101], v212 offset:21504
	v_cvt_pk_bf16_f32 v66, v66, v67
	v_cvt_pk_bf16_f32 v67, v68, v69
	v_cvt_pk_bf16_f32 v68, v70, v71
	v_cvt_pk_bf16_f32 v93, v96, v97
	v_cvt_pk_bf16_f32 v69, v72, v73
	ds_read_b128 v[70:73], v212 offset:14336
	v_pk_max_i16 v90, v90, 0
	v_pk_max_i16 v91, v91, 0
	v_pk_max_i16 v92, v92, 0
	v_pk_max_i16 v93, v93, 0
	v_pk_max_i16 v66, v66, 0
	v_pk_max_i16 v67, v67, 0
	v_pk_max_i16 v68, v68, 0
	v_pk_max_i16 v69, v69, 0
	v_cvt_pk_bf16_f32 v96, v102, v103
	s_waitcnt lgkmcnt(2)
	v_mfma_f32_32x32x16_bf16 v[2:17], v[110:113], v[90:93], v[2:17]
	v_cvt_pk_bf16_f32 v97, v104, v105
	v_cvt_pk_bf16_f32 v74, v74, v75
	v_cvt_pk_bf16_f32 v75, v76, v77
	v_cvt_pk_bf16_f32 v76, v78, v79
	v_cvt_pk_bf16_f32 v77, v80, v81
	v_pk_max_i16 v94, v94, 0
	v_pk_max_i16 v95, v95, 0
	v_pk_max_i16 v96, v96, 0
	v_pk_max_i16 v97, v97, 0
	v_pk_max_i16 v74, v74, 0
	v_pk_max_i16 v75, v75, 0
	v_pk_max_i16 v76, v76, 0
	v_pk_max_i16 v77, v77, 0
	v_mfma_f32_32x32x16_bf16 v[18:33], v[110:113], v[66:69], v[18:33]
	s_waitcnt lgkmcnt(1)
	v_mfma_f32_32x32x16_bf16 v[34:49], v[98:101], v[66:69], v[34:49]
	ds_read_b128 v[66:69], v212 offset:22528
	v_mfma_f32_32x32x16_bf16 v[50:65], v[98:101], v[90:93], v[50:65]
	s_waitcnt lgkmcnt(1)
	v_mfma_f32_32x32x16_bf16 v[2:17], v[70:73], v[94:97], v[2:17]
	v_mfma_f32_32x32x16_bf16 v[18:33], v[70:73], v[74:77], v[18:33]
	ds_read_b128 v[78:81], v212 offset:3072
	s_waitcnt lgkmcnt(1)
	v_mfma_f32_32x32x16_bf16 v[50:65], v[66:69], v[94:97], v[50:65]
	ds_read_b128 v[90:93], v174 offset:33056
	ds_read_b128 v[94:97], v174 offset:33088
	ds_read_b128 v[98:101], v174 offset:33120
	ds_read_b128 v[70:73], v174 offset:33152
	v_mfma_f32_32x32x16_bf16 v[34:49], v[66:69], v[74:77], v[34:49]
	ds_read_b128 v[66:69], v212 offset:4096
	ds_read_b128 v[74:77], v212 offset:5120
	s_waitcnt lgkmcnt(3)
	v_mfma_f32_32x32x16_bf16 v[102:117], v[78:81], v[126:129], v[86:101]
	v_mfma_f32_32x32x16_bf16 v[86:101], v[78:81], v[134:137], v[86:101]
	s_waitcnt lgkmcnt(1)
	v_mfma_f32_32x32x16_bf16 v[86:101], v[66:69], v[146:149], v[86:101]
	v_mfma_f32_32x32x16_bf16 v[102:117], v[66:69], v[122:125], v[102:117]
	ds_read_b128 v[66:69], v212 offset:6144
	s_waitcnt lgkmcnt(1)
	v_mfma_f32_32x32x16_bf16 v[86:101], v[74:77], v[142:145], v[86:101]
	v_mfma_f32_32x32x16_bf16 v[102:117], v[74:77], v[130:133], v[102:117]
	ds_read_b128 v[74:77], v212 offset:15360
	s_waitcnt lgkmcnt(1)
	v_mfma_f32_32x32x16_bf16 v[86:101], v[66:69], v[138:141], v[86:101]
	v_mfma_f32_32x32x16_bf16 v[102:117], v[66:69], v[118:121], v[102:117]
	s_nop 10
	v_cvt_pk_bf16_f32 v78, v86, v87
	v_cvt_pk_bf16_f32 v80, v90, v91
	v_cvt_pk_bf16_f32 v79, v88, v89
	v_cvt_pk_bf16_f32 v81, v92, v93
	ds_read_b128 v[86:89], v212 offset:16384
	ds_read_b128 v[90:93], v212 offset:23552
	v_cvt_pk_bf16_f32 v66, v102, v103
	v_cvt_pk_bf16_f32 v67, v104, v105
	v_cvt_pk_bf16_f32 v68, v106, v107
	v_cvt_pk_bf16_f32 v69, v108, v109
	v_pk_max_i16 v66, v66, 0
	v_pk_max_i16 v67, v67, 0
	v_pk_max_i16 v68, v68, 0
	v_pk_max_i16 v69, v69, 0
	v_pk_max_i16 v78, v78, 0
	v_pk_max_i16 v79, v79, 0
	v_pk_max_i16 v80, v80, 0
	v_pk_max_i16 v81, v81, 0
	v_cvt_pk_bf16_f32 v94, v94, v95
	s_waitcnt lgkmcnt(2)
	v_mfma_f32_32x32x16_bf16 v[18:33], v[74:77], v[78:81], v[18:33]
	v_cvt_pk_bf16_f32 v95, v96, v97
	v_cvt_pk_bf16_f32 v96, v98, v99
	v_cvt_pk_bf16_f32 v97, v100, v101
	v_pk_max_i16 v94, v94, 0
	v_pk_max_i16 v95, v95, 0
	v_pk_max_i16 v96, v96, 0
	v_pk_max_i16 v97, v97, 0
	v_mfma_f32_32x32x16_bf16 v[2:17], v[74:77], v[66:69], v[2:17]
	v_cvt_pk_bf16_f32 v74, v110, v111
	v_cvt_pk_bf16_f32 v75, v112, v113
	v_cvt_pk_bf16_f32 v76, v114, v115
	v_cvt_pk_bf16_f32 v77, v116, v117
	v_pk_max_i16 v74, v74, 0
	v_pk_max_i16 v75, v75, 0
	v_pk_max_i16 v76, v76, 0
	v_pk_max_i16 v77, v77, 0
	s_waitcnt lgkmcnt(0)
	v_mfma_f32_32x32x16_bf16 v[50:65], v[90:93], v[66:69], v[50:65]
	ds_read_b128 v[66:69], v212 offset:24576
	v_mfma_f32_32x32x16_bf16 v[34:49], v[90:93], v[78:81], v[34:49]
	ds_read_b128 v[102:105], v212 offset:7168
	v_mfma_f32_32x32x16_bf16 v[2:17], v[86:89], v[74:77], v[2:17]
	s_waitcnt lgkmcnt(1)
	v_mfma_f32_32x32x16_bf16 v[50:65], v[66:69], v[74:77], v[50:65]
	ds_read_b128 v[74:77], v174 offset:33184
	ds_read_b128 v[78:81], v174 offset:33216
	v_mfma_f32_32x32x16_bf16 v[34:49], v[66:69], v[94:97], v[34:49]
	ds_read_b128 v[66:69], v212 offset:8192
	v_mfma_f32_32x32x16_bf16 v[18:33], v[86:89], v[94:97], v[18:33]
	s_waitcnt lgkmcnt(1)
	v_mfma_f32_32x32x16_bf16 v[86:101], v[102:105], v[126:129], v[70:85]
	v_mfma_f32_32x32x16_bf16 v[70:85], v[102:105], v[134:137], v[70:85]
	ds_read_b128 v[102:105], v212 offset:9216
	v_lshlrev_b32_e32 v135, 2, v1
	v_add_u32_e32 v134, v172, v174
	s_waitcnt lgkmcnt(1)
	v_mfma_f32_32x32x16_bf16 v[86:101], v[66:69], v[122:125], v[86:101]
	v_mfma_f32_32x32x16_bf16 v[70:85], v[66:69], v[146:149], v[70:85]
	ds_read_b128 v[66:69], v212 offset:10240
	s_waitcnt lgkmcnt(1)
	v_mfma_f32_32x32x16_bf16 v[86:101], v[102:105], v[130:133], v[86:101]
	v_mfma_f32_32x32x16_bf16 v[70:85], v[102:105], v[142:145], v[70:85]
	ds_read_b128 v[102:105], v212 offset:17408
	s_waitcnt lgkmcnt(1)
	v_mfma_f32_32x32x16_bf16 v[86:101], v[66:69], v[118:121], v[86:101]
	v_mfma_f32_32x32x16_bf16 v[70:85], v[66:69], v[138:141], v[70:85]
	s_nop 10
	v_cvt_pk_bf16_f32 v68, v90, v91
	v_cvt_pk_bf16_f32 v69, v92, v93
	ds_read_b128 v[90:93], v212 offset:25600
	v_cvt_pk_bf16_f32 v66, v86, v87
	v_cvt_pk_bf16_f32 v67, v88, v89
	v_pk_max_i16 v66, v66, 0
	v_pk_max_i16 v67, v67, 0
	v_pk_max_i16 v68, v68, 0
	v_pk_max_i16 v69, v69, 0
	v_cvt_pk_bf16_f32 v70, v70, v71
	v_cvt_pk_bf16_f32 v71, v72, v73
	s_waitcnt lgkmcnt(1)
	v_mfma_f32_32x32x16_bf16 v[2:17], v[102:105], v[66:69], v[2:17]
	v_cvt_pk_bf16_f32 v72, v74, v75
	v_cvt_pk_bf16_f32 v73, v76, v77
	ds_read_b128 v[74:77], v212 offset:18432
	v_cvt_pk_bf16_f32 v86, v94, v95
	v_cvt_pk_bf16_f32 v87, v96, v97
	v_cvt_pk_bf16_f32 v88, v98, v99
	s_waitcnt lgkmcnt(1)
	v_mfma_f32_32x32x16_bf16 v[50:65], v[90:93], v[66:69], v[50:65]
	ds_read_b128 v[66:69], v212 offset:26624
	v_cvt_pk_bf16_f32 v89, v100, v101
	v_pk_max_i16 v86, v86, 0
	v_pk_max_i16 v87, v87, 0
	v_pk_max_i16 v88, v88, 0
	v_pk_max_i16 v89, v89, 0
	v_pk_max_i16 v70, v70, 0
	v_pk_max_i16 v71, v71, 0
	v_pk_max_i16 v72, v72, 0
	v_pk_max_i16 v73, v73, 0
	v_cvt_pk_bf16_f32 v78, v78, v79
	v_cvt_pk_bf16_f32 v79, v80, v81
	s_waitcnt lgkmcnt(1)
	v_mfma_f32_32x32x16_bf16 v[2:17], v[74:77], v[86:89], v[2:17]
	v_cvt_pk_bf16_f32 v80, v82, v83
	v_cvt_pk_bf16_f32 v81, v84, v85
	v_pk_max_i16 v78, v78, 0
	v_pk_max_i16 v79, v79, 0
	v_pk_max_i16 v80, v80, 0
	v_pk_max_i16 v81, v81, 0
	s_waitcnt lgkmcnt(0)
	v_mfma_f32_32x32x16_bf16 v[50:65], v[66:69], v[86:89], v[50:65]
	v_mfma_f32_32x32x16_bf16 v[34:49], v[90:93], v[70:73], v[34:49]
	s_nop 10
	v_add_f32_e32 v130, v10, v58
	v_add_f32_e32 v131, v11, v59
	v_add_f32_e32 v132, v12, v60
	v_add_f32_e32 v133, v13, v61
	v_add_f32_e32 v138, v4, v52
	v_add_f32_e32 v139, v5, v53
	v_pk_add_f32 v[140:141], v[16:17], v[64:65]
	v_pk_add_f32 v[142:143], v[8:9], v[56:57]
	v_pk_add_f32 v[144:145], v[14:15], v[62:63]
	v_pk_add_f32 v[146:147], v[6:7], v[54:55]
	v_mfma_f32_32x32x16_bf16 v[18:33], v[102:105], v[70:73], v[18:33]
	ds_read2st64_b32 v[70:71], v135 offset0:133 offset1:134
	v_add_f32_e32 v148, v2, v50
	v_add_f32_e32 v149, v3, v51
	v_add_f32_e32 v144, v146, v144
	v_add_f32_e32 v145, v147, v145
	v_pk_add_f32 v[140:141], v[142:143], v[140:141]
	v_pk_add_f32 v[132:133], v[138:139], v[132:133]
	v_pk_add_f32 v[130:131], v[148:149], v[130:131]
	v_pk_add_f32 v[132:133], v[132:133], v[140:141]
	v_pk_add_f32 v[130:131], v[130:131], v[144:145]
	v_mfma_f32_32x32x16_bf16 v[34:49], v[66:69], v[78:81], v[34:49]
	v_pk_mov_b32 v[138:139], v[130:131], v[132:133] op_sel:[1,0]
	v_mov_b32_e32 v131, v133
	s_waitcnt vmcnt(0) lgkmcnt(0)
	v_mul_f32_e32 v66, v175, v70
	v_pk_add_f32 v[130:131], v[138:139], v[130:131]
	ds_write_b32 v173, v66 offset:512
	v_mul_f32_e32 v66, v175, v71
	v_pk_add_f32 v[130:131], v[130:131], v[130:131] op_sel:[0,1] op_sel_hi:[1,0]
	s_waitcnt lgkmcnt(0)
	ds_read_b128 v[102:105], v174 offset:34560
	ds_read_b128 v[98:101], v174 offset:34592
	ds_read_b128 v[110:113], v174 offset:34624
	ds_read_b128 v[106:109], v174 offset:34656
	ds_read_b128 v[114:117], v174 offset:34688
	ds_read_b128 v[122:125], v174 offset:34720
	ds_read_b128 v[118:121], v174 offset:34752
	ds_read_b128 v[126:129], v174 offset:34784
	v_mov_b32_dpp v66, v66 quad_perm:[1,0,3,2] row_mask:0xf bank_mask:0xf bound_ctrl:1
	v_mov_b32_e32 v131, v130
	v_fmac_f32_e32 v66, v175, v71
	s_nop 0
	v_permlane32_swap_b32_e32 v130, v131
	v_add_f32_dpp v66, v66, v66 quad_perm:[2,3,0,1] row_mask:0xf bank_mask:0xf bound_ctrl:1
	v_add_f32_e32 v130, v130, v131
	v_fmamk_f32 v65, v130, 0xbc800000, v65
	v_add_f32_dpp v66, v66, v66 row_half_mirror row_mask:0xf bank_mask:0xf bound_ctrl:1
	v_fmamk_f32 v64, v130, 0xbc800000, v64
	v_fmamk_f32 v63, v130, 0xbc800000, v63
	v_fmamk_f32 v62, v130, 0xbc800000, v62
	v_fmamk_f32 v61, v130, 0xbc800000, v61
	v_fmamk_f32 v60, v130, 0xbc800000, v60
	v_fmamk_f32 v59, v130, 0xbc800000, v59
	v_fmamk_f32 v58, v130, 0xbc800000, v58
	v_fmamk_f32 v57, v130, 0xbc800000, v57
	v_fmamk_f32 v56, v130, 0xbc800000, v56
	v_fmamk_f32 v55, v130, 0xbc800000, v55
	v_fmamk_f32 v54, v130, 0xbc800000, v54
	v_fmamk_f32 v53, v130, 0xbc800000, v53
	v_fmamk_f32 v52, v130, 0xbc800000, v52
	v_fmamk_f32 v51, v130, 0xbc800000, v51
	v_fmac_f32_e32 v50, 0xbc800000, v130
	v_add_f32_dpp v66, v66, v66 row_ror:8 row_mask:0xf bank_mask:0xf bound_ctrl:1
	v_fmamk_f32 v17, v130, 0xbc800000, v17
	v_fmamk_f32 v16, v130, 0xbc800000, v16
	v_fmamk_f32 v15, v130, 0xbc800000, v15
	v_fmamk_f32 v14, v130, 0xbc800000, v14
	v_fmamk_f32 v13, v130, 0xbc800000, v13
	v_fmamk_f32 v12, v130, 0xbc800000, v12
	v_fmamk_f32 v11, v130, 0xbc800000, v11
	v_fmamk_f32 v10, v130, 0xbc800000, v10
	v_fmamk_f32 v9, v130, 0xbc800000, v9
	v_fmamk_f32 v8, v130, 0xbc800000, v8
	v_fmamk_f32 v7, v130, 0xbc800000, v7
	v_fmamk_f32 v6, v130, 0xbc800000, v6
	v_fmamk_f32 v5, v130, 0xbc800000, v5
	v_fmamk_f32 v4, v130, 0xbc800000, v4
	v_fmamk_f32 v3, v130, 0xbc800000, v3
	v_fmac_f32_e32 v2, 0xbc800000, v130
	v_pk_mul_f32 v[130:131], v[54:55], v[54:55]
	v_pk_mul_f32 v[132:133], v[62:63], v[62:63]
	v_pk_mul_f32 v[138:139], v[50:51], v[50:51]
	v_pk_mul_f32 v[140:141], v[58:59], v[58:59]
	v_pk_mul_f32 v[142:143], v[56:57], v[56:57]
	v_pk_mul_f32 v[144:145], v[64:65], v[64:65]
	v_pk_mul_f32 v[146:147], v[52:53], v[52:53]
	v_pk_mul_f32 v[148:149], v[60:61], v[60:61]
	v_mov_b32_e32 v67, v66
	v_pk_fma_f32 v[148:149], v[12:13], v[12:13], v[148:149]
	v_pk_fma_f32 v[146:147], v[4:5], v[4:5], v[146:147]
	v_pk_fma_f32 v[144:145], v[16:17], v[16:17], v[144:145]
	v_pk_fma_f32 v[142:143], v[8:9], v[8:9], v[142:143]
	v_pk_fma_f32 v[140:141], v[10:11], v[10:11], v[140:141]
	v_pk_fma_f32 v[138:139], v[2:3], v[2:3], v[138:139]
	v_pk_fma_f32 v[132:133], v[14:15], v[14:15], v[132:133]
	v_pk_fma_f32 v[130:131], v[6:7], v[6:7], v[130:131]
	v_permlane16_swap_b32_e32 v66, v67
	v_pk_add_f32 v[130:131], v[130:131], v[132:133]
	v_pk_add_f32 v[132:133], v[138:139], v[140:141]
	v_pk_add_f32 v[138:139], v[142:143], v[144:145]
	v_pk_add_f32 v[140:141], v[146:147], v[148:149]
	v_mfma_f32_32x32x16_bf16 v[18:33], v[74:77], v[78:81], v[18:33]
	v_add_f32_e32 v136, v66, v67
	ds_read_b128 v[70:73], v134 offset:512
	ds_read_b128 v[66:69], v134 offset:544
	ds_read_b128 v[78:81], v134 offset:576
	ds_read_b128 v[74:77], v134 offset:608
	ds_read_b128 v[82:85], v134 offset:640
	ds_read_b128 v[90:93], v134 offset:672
	ds_read_b128 v[86:89], v134 offset:704
	ds_read_b128 v[94:97], v134 offset:736
	v_pk_add_f32 v[138:139], v[140:141], v[138:139]
	v_pk_add_f32 v[130:131], v[132:133], v[130:131]
	s_waitcnt lgkmcnt(8)
	v_pk_mul_f32 v[140:141], v[126:127], v[62:63]
	v_pk_mov_b32 v[132:133], v[130:131], v[138:139] op_sel:[1,0]
	v_mov_b32_e32 v131, v139
	v_pk_mul_f32 v[138:139], v[122:123], v[54:55]
	v_pk_mul_f32 v[142:143], v[114:115], v[50:51]
	v_pk_mul_f32 v[144:145], v[118:119], v[58:59]
	v_pk_mul_f32 v[146:147], v[124:125], v[56:57]
	v_pk_mul_f32 v[148:149], v[128:129], v[64:65]
	v_pk_mul_f32 v[154:155], v[116:117], v[52:53]
	v_pk_mul_f32 v[156:157], v[120:121], v[60:61]
	v_pk_fma_f32 v[154:155], v[104:105], v[4:5], v[154:155]
	v_pk_fma_f32 v[156:157], v[112:113], v[12:13], v[156:157]
	v_pk_fma_f32 v[148:149], v[108:109], v[16:17], v[148:149]
	v_pk_fma_f32 v[146:147], v[100:101], v[8:9], v[146:147]
	v_pk_fma_f32 v[144:145], v[110:111], v[10:11], v[144:145]
	v_pk_fma_f32 v[142:143], v[102:103], v[2:3], v[142:143]
	v_pk_fma_f32 v[140:141], v[106:107], v[14:15], v[140:141]
	v_pk_fma_f32 v[138:139], v[98:99], v[6:7], v[138:139]
	v_pk_add_f32 v[130:131], v[132:133], v[130:131]
	v_pk_add_f32 v[138:139], v[138:139], v[140:141]
	v_pk_add_f32 v[140:141], v[142:143], v[144:145]
	v_pk_add_f32 v[142:143], v[146:147], v[148:149]
	v_pk_add_f32 v[144:145], v[154:155], v[156:157]
	v_pk_add_f32 v[132:133], v[130:131], v[130:131] op_sel:[0,1] op_sel_hi:[1,0]
	v_pk_add_f32 v[142:143], v[144:145], v[142:143]
	v_pk_add_f32 v[138:139], v[140:141], v[138:139]
	v_add_f32_e32 v133, v142, v143
	v_add_f32_e32 v130, v138, v139
	s_waitcnt lgkmcnt(2)
	v_pk_mul_f32 v[138:139], v[90:91], v[54:55]
	s_waitcnt lgkmcnt(0)
	v_pk_mul_f32 v[140:141], v[94:95], v[62:63]
	v_pk_mul_f32 v[142:143], v[82:83], v[50:51]
	v_pk_mul_f32 v[144:145], v[86:87], v[58:59]
	v_pk_mul_f32 v[146:147], v[92:93], v[56:57]
	v_pk_mul_f32 v[148:149], v[96:97], v[64:65]
	v_pk_mul_f32 v[154:155], v[84:85], v[52:53]
	v_pk_mul_f32 v[156:157], v[88:89], v[60:61]
	v_add_f32_e32 v130, v130, v133
	v_pk_fma_f32 v[156:157], v[80:81], v[12:13], v[156:157]
	v_pk_fma_f32 v[154:155], v[72:73], v[4:5], v[154:155]
	v_pk_fma_f32 v[148:149], v[76:77], v[16:17], v[148:149]
	v_pk_fma_f32 v[146:147], v[68:69], v[8:9], v[146:147]
	v_pk_fma_f32 v[144:145], v[78:79], v[10:11], v[144:145]
	v_pk_fma_f32 v[142:143], v[70:71], v[2:3], v[142:143]
	v_pk_fma_f32 v[140:141], v[74:75], v[14:15], v[140:141]
	v_pk_fma_f32 v[138:139], v[66:67], v[6:7], v[138:139]
	v_mov_b32_e32 v133, v130
	v_pk_add_f32 v[138:139], v[138:139], v[140:141]
	v_pk_add_f32 v[140:141], v[142:143], v[144:145]
	v_pk_add_f32 v[142:143], v[146:147], v[148:149]
	v_pk_add_f32 v[144:145], v[154:155], v[156:157]
	v_permlane32_swap_b32_e32 v130, v133
	v_pk_add_f32 v[142:143], v[144:145], v[142:143]
	v_add_f32_e32 v160, v130, v133
	v_pk_add_f32 v[138:139], v[140:141], v[138:139]
	v_add_f32_e32 v133, v142, v143
	v_pk_add_f32 v[140:141], v[26:27], v[42:43]
	v_pk_add_f32 v[142:143], v[28:29], v[44:45]
	v_pk_add_f32 v[144:145], v[20:21], v[36:37]
	v_pk_add_f32 v[146:147], v[32:33], v[48:49]
	v_pk_add_f32 v[148:149], v[24:25], v[40:41]
	v_pk_add_f32 v[154:155], v[30:31], v[46:47]
	v_pk_add_f32 v[156:157], v[22:23], v[38:39]
	v_pk_add_f32 v[158:159], v[18:19], v[34:35]
	v_pk_add_f32 v[154:155], v[156:157], v[154:155]
	v_pk_add_f32 v[146:147], v[148:149], v[146:147]
	v_pk_add_f32 v[142:143], v[144:145], v[142:143]
	v_pk_add_f32 v[140:141], v[158:159], v[140:141]
	v_pk_add_f32 v[142:143], v[142:143], v[146:147]
	v_pk_add_f32 v[140:141], v[140:141], v[154:155]
	v_add_f32_e32 v130, v138, v139
	v_pk_mov_b32 v[144:145], v[140:141], v[142:143] op_sel:[1,0]
	v_mov_b32_e32 v141, v143
	v_pk_add_f32 v[140:141], v[144:145], v[140:141]
	v_add_f32_e32 v133, v130, v133
	v_pk_add_f32 v[140:141], v[140:141], v[140:141] op_sel:[0,1] op_sel_hi:[1,0]
	v_mov_b32_e32 v131, v132
	v_mov_b32_e32 v130, v140
	s_nop 1
	v_permlane32_swap_b32_e32 v140, v130
	v_add_f32_e32 v130, v140, v130
	v_fmamk_f32 v49, v130, 0xbc800000, v49
	v_fmamk_f32 v48, v130, 0xbc800000, v48
	v_fmamk_f32 v47, v130, 0xbc800000, v47
	v_fmamk_f32 v46, v130, 0xbc800000, v46
	v_fmamk_f32 v45, v130, 0xbc800000, v45
	v_fmamk_f32 v44, v130, 0xbc800000, v44
	v_fmamk_f32 v43, v130, 0xbc800000, v43
	v_fmamk_f32 v42, v130, 0xbc800000, v42
	v_fmamk_f32 v41, v130, 0xbc800000, v41
	v_fmamk_f32 v40, v130, 0xbc800000, v40
	v_fmamk_f32 v39, v130, 0xbc800000, v39
	v_fmamk_f32 v38, v130, 0xbc800000, v38
	v_fmamk_f32 v37, v130, 0xbc800000, v37
	v_fmamk_f32 v36, v130, 0xbc800000, v36
	v_fmamk_f32 v35, v130, 0xbc800000, v35
	v_fmac_f32_e32 v34, 0xbc800000, v130
	v_fmamk_f32 v33, v130, 0xbc800000, v33
	v_fmamk_f32 v32, v130, 0xbc800000, v32
	v_fmamk_f32 v31, v130, 0xbc800000, v31
	v_fmamk_f32 v30, v130, 0xbc800000, v30
	v_fmamk_f32 v29, v130, 0xbc800000, v29
	v_fmamk_f32 v28, v130, 0xbc800000, v28
	v_fmamk_f32 v27, v130, 0xbc800000, v27
	v_fmamk_f32 v26, v130, 0xbc800000, v26
	v_fmamk_f32 v25, v130, 0xbc800000, v25
	v_fmamk_f32 v24, v130, 0xbc800000, v24
	v_fmamk_f32 v23, v130, 0xbc800000, v23
	v_fmamk_f32 v22, v130, 0xbc800000, v22
	v_fmamk_f32 v21, v130, 0xbc800000, v21
	v_fmamk_f32 v20, v130, 0xbc800000, v20
	v_fmamk_f32 v19, v130, 0xbc800000, v19
	v_fmac_f32_e32 v18, 0xbc800000, v130
	v_pk_mul_f32 v[140:141], v[38:39], v[38:39]
	v_pk_mul_f32 v[142:143], v[46:47], v[46:47]
	v_pk_mul_f32 v[144:145], v[34:35], v[34:35]
	v_pk_mul_f32 v[146:147], v[42:43], v[42:43]
	v_pk_mul_f32 v[148:149], v[40:41], v[40:41]
	v_pk_mul_f32 v[154:155], v[48:49], v[48:49]
	v_pk_mul_f32 v[156:157], v[36:37], v[36:37]
	v_pk_mul_f32 v[158:159], v[44:45], v[44:45]
	v_pk_fma_f32 v[156:157], v[20:21], v[20:21], v[156:157]
	v_pk_fma_f32 v[158:159], v[28:29], v[28:29], v[158:159]
	v_pk_fma_f32 v[154:155], v[32:33], v[32:33], v[154:155]
	v_pk_fma_f32 v[148:149], v[24:25], v[24:25], v[148:149]
	v_pk_fma_f32 v[146:147], v[26:27], v[26:27], v[146:147]
	v_pk_fma_f32 v[144:145], v[18:19], v[18:19], v[144:145]
	v_pk_fma_f32 v[142:143], v[30:31], v[30:31], v[142:143]
	v_pk_fma_f32 v[140:141], v[22:23], v[22:23], v[140:141]
	v_permlane32_swap_b32_e32 v132, v131
	v_pk_add_f32 v[140:141], v[140:141], v[142:143]
	v_pk_add_f32 v[142:143], v[144:145], v[146:147]
	v_pk_add_f32 v[144:145], v[148:149], v[154:155]
	v_pk_add_f32 v[146:147], v[156:157], v[158:159]
	v_pk_add_f32 v[140:141], v[142:143], v[140:141]
	v_pk_add_f32 v[144:145], v[146:147], v[144:145]
	v_pk_mul_f32 v[122:123], v[122:123], v[38:39]
	v_pk_mov_b32 v[142:143], v[140:141], v[144:145] op_sel:[1,0]
	v_mov_b32_e32 v141, v145
	v_pk_add_f32 v[140:141], v[142:143], v[140:141]
	v_pk_mul_f32 v[126:127], v[126:127], v[46:47]
	v_pk_add_f32 v[140:141], v[140:141], v[140:141] op_sel:[0,1] op_sel_hi:[1,0]
	v_pk_mul_f32 v[114:115], v[114:115], v[34:35]
	v_mov_b32_e32 v130, v140
	s_nop 1
	v_permlane32_swap_b32_e32 v140, v130
	v_mov_b32_e32 v141, v132
	v_pk_add_f32 v[130:131], v[140:141], v[130:131]
	v_pk_mul_f32 v[118:119], v[118:119], v[42:43]
	v_pk_fma_f32 v[130:131], v[130:131], s[0:1], v[152:153] op_sel_hi:[1,0,0]
	v_pk_mul_f32 v[124:125], v[124:125], v[40:41]
	v_mul_f32_e32 v132, 0x4b800000, v131
	v_cmp_gt_f32_e32 vcc, s1, v131
	v_pk_mul_f32 v[128:129], v[128:129], v[48:49]
	v_pk_mul_f32 v[116:117], v[116:117], v[36:37]
	v_pk_mul_f32 v[120:121], v[120:121], v[44:45]
	v_cndmask_b32_e32 v131, v131, v132, vcc
	v_mul_f32_e32 v132, 0x4b800000, v130
	v_cmp_gt_f32_e64 s[0:1], s1, v130
	v_pk_fma_f32 v[112:113], v[112:113], v[28:29], v[120:121]
	v_pk_fma_f32 v[104:105], v[104:105], v[20:21], v[116:117]
	v_pk_fma_f32 v[108:109], v[108:109], v[32:33], v[128:129]
	v_pk_fma_f32 v[100:101], v[100:101], v[24:25], v[124:125]
	v_pk_fma_f32 v[110:111], v[110:111], v[26:27], v[118:119]
	v_pk_fma_f32 v[102:103], v[102:103], v[18:19], v[114:115]
	v_pk_fma_f32 v[106:107], v[106:107], v[30:31], v[126:127]
	v_pk_fma_f32 v[98:99], v[98:99], v[22:23], v[122:123]
	v_rsq_f32_e32 v131, v131
	v_cndmask_b32_e64 v130, v130, v132, s[0:1]
	v_pk_add_f32 v[98:99], v[98:99], v[106:107]
	v_pk_add_f32 v[102:103], v[102:103], v[110:111]
	v_pk_add_f32 v[100:101], v[100:101], v[108:109]
	v_pk_add_f32 v[104:105], v[104:105], v[112:113]
	v_rsq_f32_e32 v132, v130
	v_pk_add_f32 v[100:101], v[104:105], v[100:101]
	v_pk_add_f32 v[98:99], v[102:103], v[98:99]
	v_mul_f32_e32 v130, 0x45800000, v131
	v_add_f32_e32 v98, v98, v99
	v_add_f32_e32 v99, v100, v101
	v_add_f32_e32 v98, v98, v99
	v_mov_b32_e32 v99, v98
	v_pk_mul_f32 v[90:91], v[90:91], v[38:39]
	v_pk_mul_f32 v[94:95], v[94:95], v[46:47]
	v_pk_mul_f32 v[82:83], v[82:83], v[34:35]
	v_pk_mul_f32 v[86:87], v[86:87], v[42:43]
	v_cndmask_b32_e32 v130, v131, v130, vcc
	v_mul_f32_e32 v131, 0x45800000, v132
	v_permlane32_swap_b32_e32 v98, v99
	v_pk_fma_f32 v[78:79], v[78:79], v[26:27], v[86:87]
	v_pk_fma_f32 v[70:71], v[70:71], v[18:19], v[82:83]
	v_pk_fma_f32 v[74:75], v[74:75], v[30:31], v[94:95]
	v_pk_fma_f32 v[66:67], v[66:67], v[22:23], v[90:91]
	v_cndmask_b32_e64 v131, v132, v131, s[0:1]
	v_add_f32_e32 v98, v98, v99
	v_pk_add_f32 v[66:67], v[66:67], v[74:75]
	v_pk_add_f32 v[70:71], v[70:71], v[78:79]
	v_mul_f32_e32 v139, v160, v130
	v_mul_f32_e32 v98, v98, v131
	v_pk_add_f32 v[66:67], v[70:71], v[66:67]
	v_cmp_gt_u32_e32 vcc, 32, v1
	v_add_f32_e32 v66, v66, v67
	v_pk_mul_f32 v[92:93], v[92:93], v[40:41]
	v_cndmask_b32_e32 v67, v98, v139, vcc
	v_add_f32_e32 v67, s12, v67
	v_pk_mul_f32 v[96:97], v[96:97], v[48:49]
	v_pk_mul_f32 v[84:85], v[84:85], v[36:37]
	v_pk_mul_f32 v[88:89], v[88:89], v[44:45]
	v_mul_f32_e32 v67, 0xbfb8aa3b, v67
	v_pk_fma_f32 v[80:81], v[80:81], v[28:29], v[88:89]
	v_pk_fma_f32 v[72:73], v[72:73], v[20:21], v[84:85]
	v_pk_fma_f32 v[76:77], v[76:77], v[32:33], v[96:97]
	v_pk_fma_f32 v[68:69], v[68:69], v[24:25], v[92:93]
	v_exp_f32_e32 v70, v67
	v_pk_add_f32 v[68:69], v[68:69], v[76:77]
	v_pk_add_f32 v[72:73], v[72:73], v[80:81]
	v_cmp_lt_i32_e64 s[0:1], 0, v151
	v_pk_add_f32 v[68:69], v[72:73], v[68:69]
	v_mov_b32_e32 v137, v136
	v_add_f32_e32 v67, v68, v69
	v_add_f32_e32 v67, v66, v67
	v_add_f32_e32 v66, 1.0, v70
	v_rcp_f32_e32 v66, v66
	v_mov_b32_e32 v69, 0xff800000
	v_mov_b32_e32 v138, v133
	v_mov_b32_e32 v68, v67
	v_cndmask_b32_e64 v70, v69, v66, s[0:1]
	v_mbcnt_lo_u32_b32 v66, -1, 0
	v_mbcnt_hi_u32_b32 v66, -1, v66
	v_permlane32_swap_b32_e32 v136, v137
	v_permlane32_swap_b32_e32 v133, v138
	v_permlane32_swap_b32_e32 v67, v68
	v_and_b32_e32 v86, 64, v66
	s_mov_b32 s14, 8
	s_mov_b32 s13, 0
	v_mov_b32_e32 v66, 0
	s_waitcnt lgkmcnt(0)
	s_nop 0
	s_nop 0
